# P1 expert-weight conversion burst of each group staggered in two cohorts (odd/even WG), one projection round apart
# baseline (speedup 1.0000x reference)
.LBB0_318:
	s_ashr_i32 s1, s30, 5
	s_mul_i32 s0, s0, s1
	s_ashr_i32 s1, s0, 31
	s_lshr_b32 s1, s1, 29
	s_add_i32 s0, s0, s1
	s_ashr_i32 s50, s0, 3
	s_and_b32 s1, s30, 1
	s_add_i32 s50, s50, s1
